# speedup vs baseline: 1.0099x; 1.0099x over previous
.LBB0_32:
	s_andn2_b64 vcc, exec, s[4:5]
	s_cbranch_vccnz .LBB0_64
	s_load_dwordx4 s[12:15], s[0:1], 0x30
	s_load_dwordx4 s[16:19], s[0:1], 0x8
	v_lshrrev_b32_e32 v39, 5, v0
	v_and_b32_e32 v46, 31, v0
	v_lshlrev_b32_e32 v1, 8, v39
	v_lshl_or_b32 v9, s2, 10, v0
	s_mov_b32 s3, 0x30d40
	v_or_b32_e32 v2, v1, v46
	v_cmp_gt_i32_e64 s[8:9], s3, v9
	v_lshlrev_b32_e32 v8, 2, v2
	v_lshlrev_b32_e32 v41, 2, v46
	v_cndmask_b32_e64 v2, 0, v9, s[8:9]
	v_ashrrev_i32_e32 v3, 31, v2
	s_waitcnt lgkmcnt(0)
	v_lshl_add_u64 v[4:5], v[2:3], 2, s[16:17]
	v_lshlrev_b64 v[2:3], 5, v[2:3]
	v_add_co_u32_e32 v6, vcc, 0xc3000, v4
	v_lshl_add_u64 v[2:3], s[18:19], 0, v[2:3]
	global_load_dword v47, v8, s[12:13]
	global_load_dword v48, v8, s[12:13] offset:128
	global_load_dword v49, v41, s[14:15] offset:128
	global_load_dword v30, v41, s[14:15] offset:256
	global_load_dword v31, v41, s[14:15] offset:384
	global_load_dword v20, v41, s[14:15] offset:512
	global_load_dword v21, v41, s[14:15] offset:640
	global_load_dword v18, v41, s[14:15] offset:768
	global_load_dword v19, v41, s[14:15] offset:896
	global_load_dword v58, v41, s[14:15]
	v_addc_co_u32_e32 v7, vcc, 0, v5, vcc
	global_load_dword v71, v[4:5], off
	global_load_dword v82, v[6:7], off offset:1280
	global_load_dwordx4 v[50:53], v[2:3], off offset:16
	global_load_dwordx4 v[54:57], v[2:3], off
	v_or_b32_e32 v2, 0x100, v9
	v_cmp_gt_i32_e64 s[6:7], s3, v2
	s_mov_b32 s10, 0xc3000
	s_load_dwordx4 s[20:23], s[0:1], 0x48
	v_cndmask_b32_e64 v2, 0, v2, s[6:7]
	v_ashrrev_i32_e32 v3, 31, v2
	v_lshl_add_u64 v[4:5], v[2:3], 2, s[16:17]
	v_lshlrev_b64 v[2:3], 5, v[2:3]
	v_add_co_u32_e32 v6, vcc, s10, v4
	v_lshl_add_u64 v[2:3], s[18:19], 0, v[2:3]
	s_nop 0
	v_addc_co_u32_e32 v7, vcc, 0, v5, vcc
	global_load_dword v69, v[4:5], off
	global_load_dword v74, v[6:7], off offset:1280
	global_load_dwordx4 v[22:25], v[2:3], off offset:16
	global_load_dwordx4 v[26:29], v[2:3], off
	v_or_b32_e32 v2, 0x200, v9
	v_cmp_gt_i32_e64 s[4:5], s3, v2
	v_or_b32_e32 v1, v1, v41
	s_nop 0
	v_cndmask_b32_e64 v2, 0, v2, s[4:5]
	v_ashrrev_i32_e32 v3, 31, v2
	v_lshl_add_u64 v[4:5], v[2:3], 2, s[16:17]
	v_lshlrev_b64 v[2:3], 5, v[2:3]
	v_add_co_u32_e32 v6, vcc, s10, v4
	v_lshl_add_u64 v[2:3], s[18:19], 0, v[2:3]
	s_nop 0
	v_addc_co_u32_e32 v7, vcc, 0, v5, vcc
	global_load_dword v65, v[4:5], off
	global_load_dword v72, v[6:7], off offset:1280
	global_load_dwordx4 v[10:13], v[2:3], off offset:16
	global_load_dwordx4 v[14:17], v[2:3], off
	v_or_b32_e32 v2, 0x300, v9
	v_cmp_gt_i32_e32 vcc, s3, v2
	s_nop 1
	v_cndmask_b32_e32 v2, 0, v2, vcc
	v_ashrrev_i32_e32 v3, 31, v2
	v_lshl_add_u64 v[4:5], v[2:3], 2, s[16:17]
	v_add_co_u32_e64 v6, s[10:11], s10, v4
	v_lshlrev_b64 v[2:3], 5, v[2:3]
	s_nop 0
	v_addc_co_u32_e64 v7, s[10:11], 0, v5, s[10:11]
	global_load_dword v61, v[4:5], off
	global_load_dword v70, v[6:7], off offset:1280
	v_lshl_add_u64 v[44:45], s[18:19], 0, v[2:3]
	global_load_dword v42, v8, s[12:13] offset:256
	global_load_dword v43, v8, s[12:13] offset:384
	global_load_dword v38, v8, s[12:13] offset:512
	global_load_dword v40, v8, s[12:13] offset:640
	global_load_dword v34, v8, s[12:13] offset:768
	global_load_dword v35, v8, s[12:13] offset:896
	s_waitcnt lgkmcnt(0)
	global_load_dword v32, v1, s[20:21]
	global_load_dword v33, v1, s[20:21] offset:128
	global_load_dword v36, v41, s[22:23]
	global_load_dword v37, v41, s[22:23] offset:128
	global_load_dwordx4 v[2:5], v[44:45], off offset:16
	global_load_dwordx4 v[6:9], v[44:45], off
	v_mbcnt_lo_u32_b32 v1, -1, 0
	v_mbcnt_hi_u32_b32 v1, -1, v1
	v_and_b32_e32 v75, 64, v1
	v_xor_b32_e32 v45, 16, v1
	s_waitcnt vmcnt(33)
	v_mul_f32_e32 v41, v48, v49
	s_waitcnt vmcnt(26)
	v_fmac_f32_e32 v41, v47, v58
	v_mov_b32_e32 v44, v41
	v_add_u32_e32 v47, 64, v75
	v_cmp_lt_i32_e64 s[10:11], v45, v47
	v_mov_b32_dpp v44, v44 quad_perm:[1,0,3,2] row_mask:0xf bank_mask:0xf
	v_add_f32_e32 v41, v41, v44
	v_mov_b32_e32 v44, v41
	s_nop 1
	v_mov_b32_dpp v44, v44 quad_perm:[2,3,0,1] row_mask:0xf bank_mask:0xf
	v_add_f32_e32 v41, v41, v44
	v_mov_b32_e32 v44, v41
	s_nop 1
	v_mov_b32_dpp v44, v44 row_half_mirror row_mask:0xf bank_mask:0xf
	v_add_f32_e32 v41, v41, v44
	v_mov_b32_e32 v44, v41
	s_nop 1
	v_mov_b32_dpp v44, v44 row_mirror row_mask:0xf bank_mask:0xf
	v_add_f32_e32 v44, v41, v44
	v_cndmask_b32_e64 v41, v1, v45, s[10:11]
	v_lshlrev_b32_e32 v41, 2, v41
	s_nop 1
	v_mov_b32_dpp v45, v44 row_bcast:15 row_mask:0xa bank_mask:0xf
	v_cmp_eq_u32_e64 s[10:11], 16, v46
	v_mov_b32_e32 v46, 0x1010
	v_mad_u32_u24 v39, v39, 20, v46
	s_and_saveexec_b64 s[12:13], s[10:11]
	s_cbranch_execz .LBB0_35
	s_waitcnt lgkmcnt(0)
	v_add_f32_e32 v44, v44, v45
	ds_write_b32 v39, v44
.LBB0_35:
	s_or_b64 exec, exec, s[12:13]
	s_waitcnt vmcnt(10)
	v_mul_f32_e32 v31, v43, v31
	v_fmac_f32_e32 v31, v42, v30
	v_mov_b32_e32 v30, v31
	s_nop 1
	v_mov_b32_dpp v30, v30 quad_perm:[1,0,3,2] row_mask:0xf bank_mask:0xf
	v_add_f32_e32 v30, v31, v30
	v_mov_b32_e32 v31, v30
	s_nop 1
	v_mov_b32_dpp v31, v31 quad_perm:[2,3,0,1] row_mask:0xf bank_mask:0xf
	v_add_f32_e32 v30, v30, v31
	v_mov_b32_e32 v31, v30
	s_nop 1
	v_mov_b32_dpp v31, v31 row_half_mirror row_mask:0xf bank_mask:0xf
	v_add_f32_e32 v30, v30, v31
	v_mov_b32_e32 v31, v30
	s_nop 1
	v_mov_b32_dpp v31, v31 row_mirror row_mask:0xf bank_mask:0xf
	v_add_f32_e32 v30, v30, v31
	s_nop 1
	v_mov_b32_dpp v31, v30 row_bcast:15 row_mask:0xa bank_mask:0xf
	s_and_saveexec_b64 s[12:13], s[10:11]
	s_cbranch_execz .LBB0_37
	s_waitcnt lgkmcnt(0)
	v_add_f32_e32 v30, v30, v31
	ds_write_b32 v39, v30 offset:4
.LBB0_37:
	s_or_b64 exec, exec, s[12:13]
	s_waitcnt vmcnt(8)
	v_mul_f32_e32 v21, v40, v21
	v_fmac_f32_e32 v21, v38, v20
	v_mov_b32_e32 v20, v21
	s_nop 1
	v_mov_b32_dpp v20, v20 quad_perm:[1,0,3,2] row_mask:0xf bank_mask:0xf
	v_add_f32_e32 v20, v21, v20
	v_mov_b32_e32 v21, v20
	s_nop 1
	v_mov_b32_dpp v21, v21 quad_perm:[2,3,0,1] row_mask:0xf bank_mask:0xf
	v_add_f32_e32 v20, v20, v21
	v_mov_b32_e32 v21, v20
	s_nop 1
	v_mov_b32_dpp v21, v21 row_half_mirror row_mask:0xf bank_mask:0xf
	v_add_f32_e32 v20, v20, v21
	v_mov_b32_e32 v21, v20
	s_nop 1
	v_mov_b32_dpp v21, v21 row_mirror row_mask:0xf bank_mask:0xf
	v_add_f32_e32 v20, v20, v21
	s_nop 1
	v_mov_b32_dpp v21, v20 row_bcast:15 row_mask:0xa bank_mask:0xf
	s_and_saveexec_b64 s[12:13], s[10:11]
	s_cbranch_execz .LBB0_39
	s_waitcnt lgkmcnt(0)
	v_add_f32_e32 v20, v20, v21
	ds_write_b32 v39, v20 offset:8
.LBB0_39:
	s_or_b64 exec, exec, s[12:13]
	s_waitcnt vmcnt(6)
	v_mul_f32_e32 v19, v35, v19
	v_fmac_f32_e32 v19, v34, v18
	v_mov_b32_e32 v18, v19
	s_nop 1
	v_mov_b32_dpp v18, v18 quad_perm:[1,0,3,2] row_mask:0xf bank_mask:0xf
	v_add_f32_e32 v18, v19, v18
	v_mov_b32_e32 v19, v18
	s_nop 1
	v_mov_b32_dpp v19, v19 quad_perm:[2,3,0,1] row_mask:0xf bank_mask:0xf
	v_add_f32_e32 v18, v18, v19
	v_mov_b32_e32 v19, v18
	s_nop 1
	v_mov_b32_dpp v19, v19 row_half_mirror row_mask:0xf bank_mask:0xf
	v_add_f32_e32 v18, v18, v19
	v_mov_b32_e32 v19, v18
	s_nop 1
	v_mov_b32_dpp v19, v19 row_mirror row_mask:0xf bank_mask:0xf
	v_add_f32_e32 v18, v18, v19
	s_nop 1
	v_mov_b32_dpp v19, v18 row_bcast:15 row_mask:0xa bank_mask:0xf
	s_and_saveexec_b64 s[12:13], s[10:11]
	s_cbranch_execz .LBB0_41
	s_waitcnt lgkmcnt(0)
	v_add_f32_e32 v18, v18, v19
	ds_write_b32 v39, v18 offset:12
.LBB0_41:
	s_or_b64 exec, exec, s[12:13]
	s_waitcnt vmcnt(2)
	v_mul_f32_e32 v18, v33, v37
	v_fmac_f32_e32 v18, v32, v36
	s_waitcnt lgkmcnt(0)
	v_mov_b32_e32 v19, v18
	s_nop 1
	v_mov_b32_dpp v19, v19 quad_perm:[1,0,3,2] row_mask:0xf bank_mask:0xf
	v_add_f32_e32 v18, v18, v19
	v_mov_b32_e32 v19, v18
	s_nop 1
	v_mov_b32_dpp v19, v19 quad_perm:[2,3,0,1] row_mask:0xf bank_mask:0xf
	v_add_f32_e32 v18, v18, v19
	v_mov_b32_e32 v19, v18
	s_nop 1
	v_mov_b32_dpp v19, v19 row_half_mirror row_mask:0xf bank_mask:0xf
	v_add_f32_e32 v18, v18, v19
	v_mov_b32_e32 v19, v18
	s_nop 1
	v_mov_b32_dpp v19, v19 row_mirror row_mask:0xf bank_mask:0xf
	v_add_f32_e32 v18, v18, v19
	s_nop 1
	v_mov_b32_dpp v19, v18 row_bcast:15 row_mask:0xa bank_mask:0xf
	s_and_saveexec_b64 s[12:13], s[10:11]
	s_cbranch_execz .LBB0_43
	s_waitcnt lgkmcnt(0)
	v_add_f32_e32 v18, v18, v19
	ds_write_b32 v39, v18 offset:16

.LBB0_64:
	s_endpgm
	s_nop 0
	s_nop 0
	s_nop 0
	s_nop 0
	s_nop 0
	s_nop 0
	s_nop 0
	s_nop 0
	s_nop 0
	s_nop 0
	s_nop 0
	s_nop 0
	s_nop 0
	s_nop 0
	s_nop 0
	s_nop 0
	s_nop 0
	s_nop 0
	s_nop 0
	s_nop 0
	s_nop 0
	s_nop 0
	s_nop 0
	s_nop 0
	s_nop 0
	s_nop 0
	s_nop 0
	s_nop 0
	s_nop 0
	s_nop 0
	s_nop 0
	s_nop 0
	s_endpgm
